# K1 kernarg loads hoisted to entry (block 0 no longer pays extra scalar round trips)
# baseline (speedup 1.0000x reference)
_Z6k_partPKiS0_PjPtS1_S1_S1_:
	s_load_dwordx8 s[36:43], s[0:1], 0x10
	s_load_dwordx4 s[28:31], s[0:1], 0x0
	s_load_dwordx2 s[6:7], s[0:1], 0x30
	s_cmp_eq_u32 s2, 0
	s_cbranch_scc0 .LBB0_6
	v_sub_u32_e32 v1, 0xd7f, v0
	v_lshrrev_b32_e32 v4, 10, v1
	v_or_b32_e32 v1, 0x400, v0
	v_lshlrev_b32_e32 v3, 2, v0
	v_mov_b32_e32 v2, 0
	v_lshlrev_b32_e32 v1, 2, v1
	s_waitcnt lgkmcnt(0)
	global_store_dword v3, v2, s[6:7]
	global_store_dword v1, v2, s[6:7]
	v_or_b32_e32 v1, 0xc00, v0
	v_or_b32_e32 v3, 0x800, v0
	v_cmp_lt_u32_e32 vcc, 2, v4
	v_cmp_lt_u32_e64 s[4:5], 1, v4
	s_and_saveexec_b64 s[8:9], s[4:5]
	s_cbranch_execz .LBB0_3
	v_lshlrev_b32_e32 v3, 2, v3
	global_store_dword v3, v2, s[6:7]

.LBB0_6:
	v_mov_b32_e32 v2, 0x12500
	v_or_b32_e32 v1, 0xfffffc00, v0
	v_lshl_add_u32 v2, v0, 2, v2
	s_mov_b64 s[0:1], 0
	v_mov_b32_e32 v3, 0
	s_movk_i32 s3, 0xbff
